# v80 + P6 rank loops: 76 redundant SGPR re-spills (v_writelane of a value just read from the same slot) replaced by s_nop 0
# speedup vs baseline: 1.0038x; 1.0038x over previous
; template <bool DRY> __device__ __forceinline__ void p6_item(Ctx& F, int item) {
;     ...
;             int rank = 0;
; #pragma unroll
;             for (int g2 = 0; g2 < 8; ++g2) {
;                 if ((gsel >> (8 * g2)) & 1ull) {
; #pragma unroll
;                     for (int jj = 0; jj < 8; ++jj) { const int e2 = 8 * g2 + jj; const unsigned oh = (unsigned)__builtin_amdgcn_readlane((int)ub, e2);
;                         rank += ((((unsigned long long)oh << 32) | (unsigned)(63 - e2)) > mykey) ? 1 : 0; } } }
.LBB0_595:
	v_readlane_b32 s0, v254, 24
	v_readlane_b32 s1, v254, 25
	s_mov_b32 s22, s0
	v_readlane_b32 s23, v149, 56
	s_nop 0
	s_nop 1
	s_nop 0
	v_cmp_gt_u64_e64 s[0:1], s[22:23], v[148:149]
	v_readlane_b32 s23, v149, 57
	s_nop 0
	v_cndmask_b32_e64 v156, 0, 1, s[0:1]
	v_readlane_b32 s0, v254, 57
	v_readlane_b32 s1, v254, 58
	s_mov_b32 s22, s0
	s_nop 0
	s_nop 1
	s_nop 0
	v_cmp_gt_u64_e64 s[0:1], s[22:23], v[148:149]
	v_readlane_b32 s23, v149, 58
	s_nop 0
	v_addc_co_u32_e64 v155, s[0:1], v155, v156, s[0:1]
	v_readlane_b32 s0, v254, 22
	v_readlane_b32 s1, v254, 23
	s_mov_b32 s22, s0
	s_nop 0
	s_nop 1
	s_nop 0
	v_cmp_gt_u64_e64 s[0:1], s[22:23], v[148:149]
	v_readlane_b32 s23, v149, 59
	s_nop 0
	v_cndmask_b32_e64 v156, 0, 1, s[0:1]
	v_readlane_b32 s0, v253, 25
	v_readlane_b32 s1, v253, 26
	s_mov_b32 s22, s0
	s_nop 0
	s_nop 1
	s_nop 0
	v_cmp_gt_u64_e64 s[0:1], s[22:23], v[148:149]
	v_readlane_b32 s23, v149, 60
	s_nop 0
	v_addc_co_u32_e64 v155, s[0:1], v155, v156, s[0:1]
	v_readlane_b32 s0, v254, 16
	v_readlane_b32 s1, v254, 17
	s_mov_b32 s22, s0
	s_nop 0
	s_nop 1
	s_nop 0
	v_cmp_gt_u64_e64 s[0:1], s[22:23], v[148:149]
	v_readlane_b32 s23, v149, 61
	s_nop 0
	v_cndmask_b32_e64 v156, 0, 1, s[0:1]
	v_readlane_b32 s0, v253, 9
	v_readlane_b32 s1, v253, 10
	s_mov_b32 s22, s0
	s_nop 0
	s_nop 1
	s_nop 0
	v_cmp_gt_u64_e64 s[0:1], s[22:23], v[148:149]
	s_nop 1
	v_addc_co_u32_e64 v155, s[0:1], v155, v156, s[0:1]
	v_readlane_b32 s1, v149, 62
	s_mov_b32 s0, s25
	s_nop 0
	v_cmp_ge_u64_e64 s[0:1], s[0:1], v[148:149]
	s_nop 1
	v_cndmask_b32_e64 v156, 0, 1, s[0:1]
	v_readlane_b32 s1, v149, 63
	s_mov_b32 s0, s25
	s_nop 0
	v_cmp_gt_u64_e64 s[0:1], s[0:1], v[148:149]
	s_nop 1
	v_addc_co_u32_e64 v155, s[0:1], v155, v156, s[0:1]

; template <bool DRY> __device__ __forceinline__ void p6_item(Ctx& F, int item) {
;     ...
;             int rank = 0;
; #pragma unroll
;             for (int g2 = 0; g2 < 8; ++g2) {
;                 if ((gsel >> (8 * g2)) & 1ull) {
; #pragma unroll
;                     for (int jj = 0; jj < 8; ++jj) { const int e2 = 8 * g2 + jj; const unsigned oh = (unsigned)__builtin_amdgcn_readlane((int)ub, e2);
;                         rank += ((((unsigned long long)oh << 32) | (unsigned)(63 - e2)) > mykey) ? 1 : 0; } } }
.LBB0_606:
	v_readlane_b32 s84, v254, 24
	v_readlane_b32 s85, v254, 25
	s_mov_b32 s0, s84
	v_readlane_b32 s85, v149, 56
	v_writelane_b32 v254, s0, 24
	s_mov_b32 s24, s78
	v_readlane_b32 s79, v149, 59
	v_writelane_b32 v254, s1, 25
	v_cmp_gt_u64_e64 s[0:1], s[84:85], v[148:149]
	v_readlane_b32 s85, v149, 57
	v_readlane_b32 s83, v149, 60
	v_cndmask_b32_e64 v155, 0, 1, s[0:1]
	v_readlane_b32 s0, v254, 57
	v_readlane_b32 s1, v254, 58
	s_mov_b32 s84, s0
	s_nop 0
	v_readlane_b32 s77, v149, 61
	s_nop 0
	s_nop 0
	v_cmp_gt_u64_e64 s[0:1], s[84:85], v[148:149]
	v_readlane_b32 s84, v254, 22
	v_readlane_b32 s85, v254, 23
	v_addc_co_u32_e64 v154, s[0:1], v154, v155, s[0:1]
	s_mov_b32 s0, s84
	v_readlane_b32 s85, v149, 58
	v_writelane_b32 v254, s0, 22
	s_nop 1
	v_writelane_b32 v254, s1, 23
	v_cmp_gt_u64_e64 s[0:1], s[84:85], v[148:149]
	s_nop 1
	v_cndmask_b32_e64 v155, 0, 1, s[0:1]
	v_readlane_b32 s0, v253, 25
	v_readlane_b32 s1, v253, 26
	s_mov_b32 s78, s0
	s_nop 0
	s_nop 1
	s_nop 0
	v_cmp_gt_u64_e64 s[0:1], s[78:79], v[148:149]
	s_mov_b32 s78, s24
	s_mov_b32 s24, s82
	v_addc_co_u32_e64 v154, s[0:1], v154, v155, s[0:1]
	v_readlane_b32 s0, v254, 16
	v_readlane_b32 s1, v254, 17
	s_mov_b32 s82, s0
	s_nop 0
	s_nop 1
	s_nop 0
	v_cmp_gt_u64_e64 s[0:1], s[82:83], v[148:149]
	s_mov_b32 s82, s24
	s_mov_b32 s24, s76
	v_cndmask_b32_e64 v155, 0, 1, s[0:1]
	v_readlane_b32 s0, v253, 9
	v_readlane_b32 s1, v253, 10
	s_mov_b32 s76, s0
	s_nop 0
	s_nop 1
	s_nop 0
	v_cmp_gt_u64_e64 s[0:1], s[76:77], v[148:149]
	s_mov_b32 s76, s24
	s_nop 0
	v_addc_co_u32_e64 v154, s[0:1], v154, v155, s[0:1]
	v_readlane_b32 s1, v149, 62
	s_mov_b32 s0, s25
	s_nop 0
	v_cmp_ge_u64_e64 s[0:1], s[0:1], v[148:149]
	s_nop 1
	v_cndmask_b32_e64 v155, 0, 1, s[0:1]
	v_readlane_b32 s1, v149, 63
	s_mov_b32 s0, s25
	s_nop 0
	v_cmp_gt_u64_e64 s[0:1], s[0:1], v[148:149]
	s_nop 1
	v_addc_co_u32_e64 v154, s[0:1], v154, v155, s[0:1]

; template <bool DRY> __device__ __forceinline__ void p6_item(Ctx& F, int item) {
;     ...
;             int rank = 0;
; #pragma unroll
;             for (int g2 = 0; g2 < 8; ++g2) {
;                 if ((gsel >> (8 * g2)) & 1ull) {
; #pragma unroll
;                     for (int jj = 0; jj < 8; ++jj) { const int e2 = 8 * g2 + jj; const unsigned oh = (unsigned)__builtin_amdgcn_readlane((int)ub, e2);
;                         rank += ((((unsigned long long)oh << 32) | (unsigned)(63 - e2)) > mykey) ? 1 : 0; } } }
.LBB0_609:
	v_readlane_b32 s91, v149, 0
	v_readlane_b32 s23, v149, 1
	v_readlane_b32 s87, v149, 2
	v_cmp_gt_u64_e64 s[0:1], s[90:91], v[148:149]
	v_readlane_b32 s97, v149, 3
	v_readlane_b32 s95, v149, 4
	v_cndmask_b32_e64 v155, 0, 1, s[0:1]
	v_readlane_b32 s0, v255, 14
	v_readlane_b32 s1, v255, 15
	s_mov_b32 s22, s0
	s_nop 0
	v_readlane_b32 s5, v149, 5
	v_readlane_b32 s69, v149, 6
	s_nop 0
	v_cmp_gt_u64_e64 s[0:1], s[22:23], v[148:149]
	v_readlane_b32 s23, v149, 7
	s_nop 0
	v_addc_co_u32_e64 v155, s[0:1], 0, v155, s[0:1]
	v_cmp_gt_u64_e64 s[0:1], s[86:87], v[148:149]
	s_nop 1
	v_cndmask_b32_e64 v156, 0, 1, s[0:1]
	v_cmp_gt_u64_e64 s[0:1], s[96:97], v[148:149]
	s_nop 1
	v_addc_co_u32_e64 v155, s[0:1], v155, v156, s[0:1]
	v_cmp_gt_u64_e64 s[0:1], s[94:95], v[148:149]
	s_nop 1
	v_cndmask_b32_e64 v156, 0, 1, s[0:1]
	v_cmp_gt_u64_e64 s[0:1], s[4:5], v[148:149]
	s_nop 1
	v_addc_co_u32_e64 v155, s[0:1], v155, v156, s[0:1]
	v_cmp_gt_u64_e64 s[0:1], s[68:69], v[148:149]
	s_nop 1
	v_cndmask_b32_e64 v156, 0, 1, s[0:1]
	v_readlane_b32 s0, v254, 20
	v_readlane_b32 s1, v254, 21
	s_mov_b32 s22, s0
	s_nop 0
	s_nop 1
	s_nop 0
	v_cmp_gt_u64_e64 s[0:1], s[22:23], v[148:149]
	s_nop 1
	v_addc_co_u32_e64 v155, s[0:1], v155, v156, s[0:1]
	s_and_b32 s24, vcc_lo, 0x100
	s_cmp_eq_u64 s[24:25], 0
	s_cbranch_scc1 .LBB0_589
.LBB0_610:
	v_readlane_b32 s21, v149, 8
	v_readlane_b32 s39, v149, 9
	v_readlane_b32 s73, v149, 10
	v_cmp_gt_u64_e64 s[0:1], s[20:21], v[148:149]
	v_readlane_b32 s93, v149, 11
	v_readlane_b32 s29, v149, 12
	v_cndmask_b32_e64 v156, 0, 1, s[0:1]
	v_cmp_gt_u64_e64 s[0:1], s[38:39], v[148:149]
	v_readlane_b32 s31, v149, 13
	v_readlane_b32 s9, v149, 14
	v_addc_co_u32_e64 v155, s[0:1], v155, v156, s[0:1]
	v_cmp_gt_u64_e64 s[0:1], s[72:73], v[148:149]
	v_readlane_b32 s23, v149, 15
	s_nop 0
	v_cndmask_b32_e64 v156, 0, 1, s[0:1]
	v_cmp_gt_u64_e64 s[0:1], s[92:93], v[148:149]
	s_nop 1
	v_addc_co_u32_e64 v155, s[0:1], v155, v156, s[0:1]
	v_cmp_gt_u64_e64 s[0:1], s[28:29], v[148:149]
	s_nop 1
	v_cndmask_b32_e64 v156, 0, 1, s[0:1]
	v_cmp_gt_u64_e64 s[0:1], s[30:31], v[148:149]
	s_nop 1
	v_addc_co_u32_e64 v155, s[0:1], v155, v156, s[0:1]
	v_cmp_gt_u64_e64 s[0:1], s[8:9], v[148:149]
	s_nop 1
	v_cndmask_b32_e64 v156, 0, 1, s[0:1]
	v_readlane_b32 s0, v253, 41
	v_readlane_b32 s1, v253, 42
	s_mov_b32 s22, s0
	s_nop 0
	s_nop 1
	s_nop 0
	v_cmp_gt_u64_e64 s[0:1], s[22:23], v[148:149]
	s_nop 1
	v_addc_co_u32_e64 v155, s[0:1], v155, v156, s[0:1]
	s_and_b32 s24, vcc_lo, 0x10000
	s_cmp_eq_u64 s[24:25], 0
	s_cbranch_scc1 .LBB0_590
.LBB0_611:
	v_readlane_b32 s0, v254, 42
	v_readlane_b32 s1, v254, 43
	s_mov_b32 s22, s0
	v_readlane_b32 s23, v149, 16
	s_nop 0
	v_readlane_b32 s11, v149, 17
	v_readlane_b32 s15, v149, 18
	s_nop 0
	v_cmp_gt_u64_e64 s[0:1], s[22:23], v[148:149]
	v_readlane_b32 s19, v149, 19
	v_readlane_b32 s27, v149, 20
	v_cndmask_b32_e64 v156, 0, 1, s[0:1]
	v_cmp_gt_u64_e64 s[0:1], s[10:11], v[148:149]
	v_readlane_b32 s37, v149, 21
	v_readlane_b32 s43, v149, 22
	v_addc_co_u32_e64 v155, s[0:1], v155, v156, s[0:1]
	v_cmp_gt_u64_e64 s[0:1], s[14:15], v[148:149]
	v_readlane_b32 s23, v149, 23
	s_nop 0
	v_cndmask_b32_e64 v156, 0, 1, s[0:1]
	v_cmp_gt_u64_e64 s[0:1], s[18:19], v[148:149]
	s_nop 1
	v_addc_co_u32_e64 v155, s[0:1], v155, v156, s[0:1]
	v_cmp_gt_u64_e64 s[0:1], s[26:27], v[148:149]
	s_nop 1
	v_cndmask_b32_e64 v156, 0, 1, s[0:1]
	v_cmp_gt_u64_e64 s[0:1], s[36:37], v[148:149]
	s_nop 1
	v_addc_co_u32_e64 v155, s[0:1], v155, v156, s[0:1]
	v_cmp_gt_u64_e64 s[0:1], s[42:43], v[148:149]
	s_nop 1
	v_cndmask_b32_e64 v156, 0, 1, s[0:1]
	v_readlane_b32 s0, v255, 12
	v_readlane_b32 s1, v255, 13
	s_mov_b32 s22, s0
	s_nop 0
	s_nop 1
	s_nop 0
	v_cmp_gt_u64_e64 s[0:1], s[22:23], v[148:149]
	s_nop 1
	v_addc_co_u32_e64 v155, s[0:1], v155, v156, s[0:1]
	s_and_b32 s24, vcc_lo, 0x1000000
	s_cmp_eq_u64 s[24:25], 0
	s_cbranch_scc1 .LBB0_591
.LBB0_612:
	v_readlane_b32 s0, v254, 38
	v_readlane_b32 s1, v254, 39
	s_mov_b32 s22, s0
	v_readlane_b32 s23, v149, 24
	s_nop 0
	v_readlane_b32 s47, v149, 25
	v_readlane_b32 s51, v149, 26
	s_nop 0
	v_cmp_gt_u64_e64 s[0:1], s[22:23], v[148:149]
	v_readlane_b32 s53, v149, 27
	v_readlane_b32 s57, v149, 28
	v_cndmask_b32_e64 v156, 0, 1, s[0:1]
	v_cmp_gt_u64_e64 s[0:1], s[46:47], v[148:149]
	v_readlane_b32 s61, v149, 29
	v_readlane_b32 s65, v149, 30
	v_addc_co_u32_e64 v155, s[0:1], v155, v156, s[0:1]
	v_cmp_gt_u64_e64 s[0:1], s[50:51], v[148:149]
	v_readlane_b32 s23, v149, 31
	s_nop 0
	v_cndmask_b32_e64 v156, 0, 1, s[0:1]
	v_cmp_gt_u64_e64 s[0:1], s[52:53], v[148:149]
	s_nop 1
	v_addc_co_u32_e64 v155, s[0:1], v155, v156, s[0:1]
	v_cmp_gt_u64_e64 s[0:1], s[56:57], v[148:149]
	s_nop 1
	v_cndmask_b32_e64 v156, 0, 1, s[0:1]
	v_cmp_gt_u64_e64 s[0:1], s[60:61], v[148:149]
	s_nop 1
	v_addc_co_u32_e64 v155, s[0:1], v155, v156, s[0:1]
	v_cmp_gt_u64_e64 s[0:1], s[64:65], v[148:149]
	s_nop 1
	v_cndmask_b32_e64 v156, 0, 1, s[0:1]
	v_readlane_b32 s0, v254, 18
	v_readlane_b32 s1, v254, 19
	s_mov_b32 s22, s0
	s_nop 0
	s_nop 1
	s_nop 0
	v_cmp_gt_u64_e64 s[0:1], s[22:23], v[148:149]
	s_nop 1
	v_addc_co_u32_e64 v155, s[0:1], v155, v156, s[0:1]
	s_and_b32 s1, vcc_hi, 1
	s_mov_b32 s0, s25
	s_cmp_eq_u64 s[0:1], 0
	s_cbranch_scc1 .LBB0_592
; template <bool DRY> __device__ __forceinline__ void p6_item(Ctx& F, int item) {
;     ...
;             int rank = 0;
; #pragma unroll
;             for (int g2 = 0; g2 < 8; ++g2) {
;                 if ((gsel >> (8 * g2)) & 1ull) {
; #pragma unroll
;                     for (int jj = 0; jj < 8; ++jj) { const int e2 = 8 * g2 + jj; const unsigned oh = (unsigned)__builtin_amdgcn_readlane((int)ub, e2);
;                         rank += ((((unsigned long long)oh << 32) | (unsigned)(63 - e2)) > mykey) ? 1 : 0; } } }
.LBB0_613:
	v_readlane_b32 s0, v254, 34
	v_readlane_b32 s1, v254, 35
	s_mov_b32 s22, s0
	v_readlane_b32 s23, v149, 32
	s_nop 0
	v_readlane_b32 s63, v149, 33
	v_readlane_b32 s59, v149, 34
	s_nop 0
	v_cmp_gt_u64_e64 s[0:1], s[22:23], v[148:149]
	v_readlane_b32 s55, v149, 35
	v_readlane_b32 s23, v149, 36
	v_cndmask_b32_e64 v156, 0, 1, s[0:1]
	v_cmp_gt_u64_e64 s[0:1], s[62:63], v[148:149]
	v_readlane_b32 s49, v149, 37
	v_readlane_b32 s45, v149, 38
	v_addc_co_u32_e64 v155, s[0:1], v155, v156, s[0:1]
	v_cmp_gt_u64_e64 s[0:1], s[58:59], v[148:149]
	s_nop 1
	v_cndmask_b32_e64 v156, 0, 1, s[0:1]
	v_cmp_gt_u64_e64 s[0:1], s[54:55], v[148:149]
	s_nop 1
	v_addc_co_u32_e64 v155, s[0:1], v155, v156, s[0:1]
	v_readlane_b32 s0, v255, 4
	v_readlane_b32 s1, v255, 5
	s_mov_b32 s22, s0
	s_nop 0
	s_nop 1
	s_nop 0
	v_cmp_gt_u64_e64 s[0:1], s[22:23], v[148:149]
	v_readlane_b32 s23, v149, 39
	s_nop 0
	v_cndmask_b32_e64 v156, 0, 1, s[0:1]
	v_cmp_gt_u64_e64 s[0:1], s[48:49], v[148:149]
	s_nop 1
	v_addc_co_u32_e64 v155, s[0:1], v155, v156, s[0:1]
	v_cmp_gt_u64_e64 s[0:1], s[44:45], v[148:149]
	s_nop 1
	v_cndmask_b32_e64 v156, 0, 1, s[0:1]
	v_readlane_b32 s0, v255, 10
	v_readlane_b32 s1, v255, 11
	s_mov_b32 s22, s0
	s_nop 0
	s_nop 1
	s_nop 0
	v_cmp_gt_u64_e64 s[0:1], s[22:23], v[148:149]
	s_nop 1
	v_addc_co_u32_e64 v155, s[0:1], v155, v156, s[0:1]
	s_and_b32 s1, vcc_hi, 0x100
	s_mov_b32 s0, s25
	s_cmp_eq_u64 s[0:1], 0
	s_cbranch_scc1 .LBB0_593
.LBB0_614:
	v_readlane_b32 s0, v254, 30
	v_readlane_b32 s1, v254, 31
	s_mov_b32 s22, s0
	v_readlane_b32 s23, v149, 40
	s_nop 0
	v_readlane_b32 s41, v149, 41
	v_readlane_b32 s35, v149, 42
	s_nop 0
	v_cmp_gt_u64_e64 s[0:1], s[22:23], v[148:149]
	v_readlane_b32 s3, v149, 43
	v_readlane_b32 s17, v149, 44
	v_cndmask_b32_e64 v156, 0, 1, s[0:1]
	v_cmp_gt_u64_e64 s[0:1], s[40:41], v[148:149]
	v_readlane_b32 s13, v149, 45
	v_readlane_b32 s23, v149, 46
	v_addc_co_u32_e64 v155, s[0:1], v155, v156, s[0:1]
	v_cmp_gt_u64_e64 s[0:1], s[34:35], v[148:149]
	v_readlane_b32 s83, v149, 47
	s_nop 0
	v_cndmask_b32_e64 v156, 0, 1, s[0:1]
	v_cmp_gt_u64_e64 s[0:1], s[2:3], v[148:149]
	s_nop 1
	v_addc_co_u32_e64 v155, s[0:1], v155, v156, s[0:1]
	v_cmp_gt_u64_e64 s[0:1], s[16:17], v[148:149]
	s_nop 1
	v_cndmask_b32_e64 v156, 0, 1, s[0:1]
	v_cmp_gt_u64_e64 s[0:1], s[12:13], v[148:149]
	s_nop 1
	v_addc_co_u32_e64 v155, s[0:1], v155, v156, s[0:1]
	v_readlane_b32 s0, v254, 60
	v_readlane_b32 s1, v254, 61
	s_mov_b32 s22, s0
	s_nop 0
	s_nop 1
	s_nop 0
	v_cmp_gt_u64_e64 s[0:1], s[22:23], v[148:149]
	s_nop 1
	v_cndmask_b32_e64 v156, 0, 1, s[0:1]
	v_cmp_gt_u64_e64 s[0:1], s[82:83], v[148:149]
	s_nop 1
	v_addc_co_u32_e64 v155, s[0:1], v155, v156, s[0:1]
	s_and_b32 s1, vcc_hi, 0x10000
	s_mov_b32 s0, s25
	s_cmp_eq_u64 s[0:1], 0
	s_cbranch_scc1 .LBB0_594
.LBB0_615:
	v_readlane_b32 s77, v149, 48
	v_readlane_b32 s7, v149, 49
	v_readlane_b32 s23, v149, 50
	v_cmp_gt_u64_e64 s[0:1], s[76:77], v[148:149]
	v_readlane_b32 s81, v149, 51
	v_readlane_b32 s71, v149, 53
	v_cndmask_b32_e64 v156, 0, 1, s[0:1]
	v_cmp_gt_u64_e64 s[0:1], s[6:7], v[148:149]
	v_readlane_b32 s89, v149, 54
	v_readlane_b32 s79, v149, 55
	v_addc_co_u32_e64 v155, s[0:1], v155, v156, s[0:1]
	v_readlane_b32 s0, v255, 6
	v_readlane_b32 s1, v255, 7
	s_mov_b32 s22, s0
	s_nop 0
	s_nop 1
	s_nop 0
	v_cmp_gt_u64_e64 s[0:1], s[22:23], v[148:149]
	v_readlane_b32 s23, v149, 52
	s_nop 0
	v_cndmask_b32_e64 v156, 0, 1, s[0:1]
	v_cmp_gt_u64_e64 s[0:1], s[80:81], v[148:149]
	s_nop 1
	v_addc_co_u32_e64 v155, s[0:1], v155, v156, s[0:1]
	v_readlane_b32 s0, v255, 8
	v_readlane_b32 s1, v255, 9
	s_mov_b32 s22, s0
	s_nop 0
	s_nop 1
	s_nop 0
	v_cmp_gt_u64_e64 s[0:1], s[22:23], v[148:149]
	s_nop 1
	v_cndmask_b32_e64 v156, 0, 1, s[0:1]
	v_cmp_gt_u64_e64 s[0:1], s[70:71], v[148:149]
	s_nop 1
	v_addc_co_u32_e64 v155, s[0:1], v155, v156, s[0:1]
	v_cmp_gt_u64_e64 s[0:1], s[88:89], v[148:149]
	s_nop 1
	v_cndmask_b32_e64 v156, 0, 1, s[0:1]
	v_cmp_gt_u64_e64 s[0:1], s[78:79], v[148:149]
	s_nop 1
	v_addc_co_u32_e64 v155, s[0:1], v155, v156, s[0:1]
	s_and_b32 s1, vcc_hi, 0x1000000
	s_mov_b32 s0, s25
	s_cmp_eq_u64 s[0:1], 0
	s_cbranch_scc0 .LBB0_595
	s_branch .LBB0_596
.LBB0_616:
	v_readlane_b32 s91, v149, 0
	v_readlane_b32 s85, v149, 1
	v_readlane_b32 s87, v149, 2
	v_cmp_gt_u64_e64 s[0:1], s[90:91], v[148:149]
	v_readlane_b32 s97, v149, 3
	v_readlane_b32 s95, v149, 4
	v_cndmask_b32_e64 v154, 0, 1, s[0:1]
	v_readlane_b32 s0, v255, 14
	v_readlane_b32 s1, v255, 15
	s_mov_b32 s84, s0
	s_nop 0
	v_readlane_b32 s5, v149, 5
	v_readlane_b32 s69, v149, 6
	s_nop 0
	v_cmp_gt_u64_e64 s[0:1], s[84:85], v[148:149]
	s_mov_b32 s24, s90
	v_readlane_b32 s91, v149, 7
	v_addc_co_u32_e64 v154, s[0:1], 0, v154, s[0:1]
	v_cmp_gt_u64_e64 s[0:1], s[86:87], v[148:149]
	s_nop 1
	v_cndmask_b32_e64 v155, 0, 1, s[0:1]
	v_cmp_gt_u64_e64 s[0:1], s[96:97], v[148:149]
	s_nop 1
	v_addc_co_u32_e64 v154, s[0:1], v154, v155, s[0:1]
	v_cmp_gt_u64_e64 s[0:1], s[94:95], v[148:149]
	s_nop 1
	v_cndmask_b32_e64 v155, 0, 1, s[0:1]
	v_cmp_gt_u64_e64 s[0:1], s[4:5], v[148:149]
	s_nop 1
	v_addc_co_u32_e64 v154, s[0:1], v154, v155, s[0:1]
	v_cmp_gt_u64_e64 s[0:1], s[68:69], v[148:149]
	s_nop 1
	v_cndmask_b32_e64 v155, 0, 1, s[0:1]
	v_readlane_b32 s0, v254, 20
	v_readlane_b32 s1, v254, 21
	s_mov_b32 s90, s0
	s_nop 0
	s_nop 1
	s_nop 0
	v_cmp_gt_u64_e64 s[0:1], s[90:91], v[148:149]
	s_mov_b32 s90, s24
	s_nop 0
	v_addc_co_u32_e64 v154, s[0:1], v154, v155, s[0:1]
	s_and_b32 s24, vcc_lo, 0x100
	s_cmp_eq_u64 s[24:25], 0
	s_cbranch_scc1 .LBB0_600
; template <bool DRY> __device__ __forceinline__ void p6_item(Ctx& F, int item) {
;     ...
;             int rank = 0;
; #pragma unroll
;             for (int g2 = 0; g2 < 8; ++g2) {
;                 if ((gsel >> (8 * g2)) & 1ull) {
; #pragma unroll
;                     for (int jj = 0; jj < 8; ++jj) { const int e2 = 8 * g2 + jj; const unsigned oh = (unsigned)__builtin_amdgcn_readlane((int)ub, e2);
;                         rank += ((((unsigned long long)oh << 32) | (unsigned)(63 - e2)) > mykey) ? 1 : 0; } } }
.LBB0_617:
	v_readlane_b32 s21, v149, 8
	v_readlane_b32 s39, v149, 9
	v_readlane_b32 s73, v149, 10
	v_cmp_gt_u64_e64 s[0:1], s[20:21], v[148:149]
	v_readlane_b32 s93, v149, 11
	v_readlane_b32 s29, v149, 12
	v_cndmask_b32_e64 v155, 0, 1, s[0:1]
	v_cmp_gt_u64_e64 s[0:1], s[38:39], v[148:149]
	v_readlane_b32 s31, v149, 13
	v_readlane_b32 s9, v149, 14
	v_addc_co_u32_e64 v154, s[0:1], v154, v155, s[0:1]
	v_cmp_gt_u64_e64 s[0:1], s[72:73], v[148:149]
	s_mov_b32 s24, s80
	v_readlane_b32 s81, v149, 15
	v_cndmask_b32_e64 v155, 0, 1, s[0:1]
	v_cmp_gt_u64_e64 s[0:1], s[92:93], v[148:149]
	s_nop 1
	v_addc_co_u32_e64 v154, s[0:1], v154, v155, s[0:1]
	v_cmp_gt_u64_e64 s[0:1], s[28:29], v[148:149]
	s_nop 1
	v_cndmask_b32_e64 v155, 0, 1, s[0:1]
	v_cmp_gt_u64_e64 s[0:1], s[30:31], v[148:149]
	s_nop 1
	v_addc_co_u32_e64 v154, s[0:1], v154, v155, s[0:1]
	v_cmp_gt_u64_e64 s[0:1], s[8:9], v[148:149]
	s_nop 1
	v_cndmask_b32_e64 v155, 0, 1, s[0:1]
	v_readlane_b32 s0, v253, 41
	v_readlane_b32 s1, v253, 42
	s_mov_b32 s80, s0
	s_nop 0
	s_nop 1
	s_nop 0
	v_cmp_gt_u64_e64 s[0:1], s[80:81], v[148:149]
	s_mov_b32 s80, s24
	s_nop 0
	v_addc_co_u32_e64 v154, s[0:1], v154, v155, s[0:1]
	s_and_b32 s24, vcc_lo, 0x10000
	s_cmp_eq_u64 s[24:25], 0
	s_cbranch_scc1 .LBB0_601
.LBB0_618:
	v_readlane_b32 s0, v254, 42
	v_readlane_b32 s1, v254, 43
	s_mov_b32 s84, s0
	v_readlane_b32 s85, v149, 16
	s_nop 0
	v_readlane_b32 s11, v149, 17
	v_readlane_b32 s15, v149, 18
	s_nop 0
	v_cmp_gt_u64_e64 s[0:1], s[84:85], v[148:149]
	v_readlane_b32 s19, v149, 19
	v_readlane_b32 s27, v149, 20
	v_cndmask_b32_e64 v155, 0, 1, s[0:1]
	v_cmp_gt_u64_e64 s[0:1], s[10:11], v[148:149]
	v_readlane_b32 s37, v149, 21
	v_readlane_b32 s43, v149, 22
	v_addc_co_u32_e64 v154, s[0:1], v154, v155, s[0:1]
	v_cmp_gt_u64_e64 s[0:1], s[14:15], v[148:149]
	v_readlane_b32 s85, v149, 23
	s_nop 0
	v_cndmask_b32_e64 v155, 0, 1, s[0:1]
	v_cmp_gt_u64_e64 s[0:1], s[18:19], v[148:149]
	s_nop 1
	v_addc_co_u32_e64 v154, s[0:1], v154, v155, s[0:1]
	v_cmp_gt_u64_e64 s[0:1], s[26:27], v[148:149]
	s_nop 1
	v_cndmask_b32_e64 v155, 0, 1, s[0:1]
	v_cmp_gt_u64_e64 s[0:1], s[36:37], v[148:149]
	s_nop 1
	v_addc_co_u32_e64 v154, s[0:1], v154, v155, s[0:1]
	v_cmp_gt_u64_e64 s[0:1], s[42:43], v[148:149]
	s_nop 1
	v_cndmask_b32_e64 v155, 0, 1, s[0:1]
	v_readlane_b32 s0, v255, 12
	v_readlane_b32 s1, v255, 13
	s_mov_b32 s84, s0
	s_nop 0
	s_nop 1
	s_nop 0
	v_cmp_gt_u64_e64 s[0:1], s[84:85], v[148:149]
	s_nop 1
	v_addc_co_u32_e64 v154, s[0:1], v154, v155, s[0:1]
	s_and_b32 s24, vcc_lo, 0x1000000
	s_cmp_eq_u64 s[24:25], 0
	s_cbranch_scc1 .LBB0_602
.LBB0_619:
	v_readlane_b32 s0, v254, 38
	v_readlane_b32 s1, v254, 39
	s_mov_b32 s84, s0
	v_readlane_b32 s85, v149, 24
	s_nop 0
	v_readlane_b32 s47, v149, 25
	v_readlane_b32 s51, v149, 26
	s_nop 0
	v_cmp_gt_u64_e64 s[0:1], s[84:85], v[148:149]
	v_readlane_b32 s53, v149, 27
	v_readlane_b32 s57, v149, 28
	v_cndmask_b32_e64 v155, 0, 1, s[0:1]
	v_cmp_gt_u64_e64 s[0:1], s[46:47], v[148:149]
	v_readlane_b32 s61, v149, 29
	v_readlane_b32 s65, v149, 30
	v_addc_co_u32_e64 v154, s[0:1], v154, v155, s[0:1]
	v_cmp_gt_u64_e64 s[0:1], s[50:51], v[148:149]
	s_mov_b32 s24, s88
	v_readlane_b32 s89, v149, 31
	v_cndmask_b32_e64 v155, 0, 1, s[0:1]
	v_cmp_gt_u64_e64 s[0:1], s[52:53], v[148:149]
	s_nop 1
	v_addc_co_u32_e64 v154, s[0:1], v154, v155, s[0:1]
	v_cmp_gt_u64_e64 s[0:1], s[56:57], v[148:149]
	s_nop 1
	v_cndmask_b32_e64 v155, 0, 1, s[0:1]
	v_cmp_gt_u64_e64 s[0:1], s[60:61], v[148:149]
	s_nop 1
	v_addc_co_u32_e64 v154, s[0:1], v154, v155, s[0:1]
	v_cmp_gt_u64_e64 s[0:1], s[64:65], v[148:149]
	s_nop 1
	v_cndmask_b32_e64 v155, 0, 1, s[0:1]
	v_readlane_b32 s0, v254, 18
	v_readlane_b32 s1, v254, 19
	s_mov_b32 s88, s0
	s_nop 0
	s_nop 1
	s_nop 0
	v_cmp_gt_u64_e64 s[0:1], s[88:89], v[148:149]
	s_mov_b32 s88, s24
	s_nop 0
	v_addc_co_u32_e64 v154, s[0:1], v154, v155, s[0:1]
	s_and_b32 s1, vcc_hi, 1
	s_mov_b32 s0, s25
	s_cmp_eq_u64 s[0:1], 0
	s_cbranch_scc1 .LBB0_603
; template <bool DRY> __device__ __forceinline__ void p6_item(Ctx& F, int item) {
;     ...
;             int rank = 0;
; #pragma unroll
;             for (int g2 = 0; g2 < 8; ++g2) {
;                 if ((gsel >> (8 * g2)) & 1ull) {
; #pragma unroll
;                     for (int jj = 0; jj < 8; ++jj) { const int e2 = 8 * g2 + jj; const unsigned oh = (unsigned)__builtin_amdgcn_readlane((int)ub, e2);
;                         rank += ((((unsigned long long)oh << 32) | (unsigned)(63 - e2)) > mykey) ? 1 : 0; } } }
.LBB0_620:
	v_readlane_b32 s0, v254, 34
	v_readlane_b32 s1, v254, 35
	s_mov_b32 s84, s0
	v_readlane_b32 s85, v149, 32
	s_nop 0
	v_readlane_b32 s63, v149, 33
	v_readlane_b32 s59, v149, 34
	s_nop 0
	v_cmp_gt_u64_e64 s[0:1], s[84:85], v[148:149]
	v_readlane_b32 s55, v149, 35
	v_readlane_b32 s85, v149, 36
	v_cndmask_b32_e64 v155, 0, 1, s[0:1]
	v_cmp_gt_u64_e64 s[0:1], s[62:63], v[148:149]
	v_readlane_b32 s49, v149, 37
	v_readlane_b32 s45, v149, 38
	v_addc_co_u32_e64 v154, s[0:1], v154, v155, s[0:1]
	v_cmp_gt_u64_e64 s[0:1], s[58:59], v[148:149]
	s_nop 1
	v_cndmask_b32_e64 v155, 0, 1, s[0:1]
	v_cmp_gt_u64_e64 s[0:1], s[54:55], v[148:149]
	s_nop 1
	v_addc_co_u32_e64 v154, s[0:1], v154, v155, s[0:1]
	v_readlane_b32 s0, v255, 4
	v_readlane_b32 s1, v255, 5
	s_mov_b32 s84, s0
	s_nop 0
	s_nop 1
	s_nop 0
	v_cmp_gt_u64_e64 s[0:1], s[84:85], v[148:149]
	v_readlane_b32 s85, v149, 39
	s_nop 0
	v_cndmask_b32_e64 v155, 0, 1, s[0:1]
	v_cmp_gt_u64_e64 s[0:1], s[48:49], v[148:149]
	s_nop 1
	v_addc_co_u32_e64 v154, s[0:1], v154, v155, s[0:1]
	v_cmp_gt_u64_e64 s[0:1], s[44:45], v[148:149]
	s_nop 1
	v_cndmask_b32_e64 v155, 0, 1, s[0:1]
	v_readlane_b32 s0, v255, 10
	v_readlane_b32 s1, v255, 11
	s_mov_b32 s84, s0
	s_nop 0
	s_nop 1
	s_nop 0
	v_cmp_gt_u64_e64 s[0:1], s[84:85], v[148:149]
	s_nop 1
	v_addc_co_u32_e64 v154, s[0:1], v154, v155, s[0:1]
	s_and_b32 s1, vcc_hi, 0x100
	s_mov_b32 s0, s25
	s_cmp_eq_u64 s[0:1], 0
	s_cbranch_scc1 .LBB0_604
.LBB0_621:
	v_readlane_b32 s0, v254, 30
	v_readlane_b32 s1, v254, 31
	s_mov_b32 s84, s0
	v_readlane_b32 s85, v149, 40
	s_nop 0
	v_readlane_b32 s41, v149, 41
	v_readlane_b32 s35, v149, 42
	s_nop 0
	v_cmp_gt_u64_e64 s[0:1], s[84:85], v[148:149]
	v_readlane_b32 s3, v149, 43
	v_readlane_b32 s17, v149, 44
	v_cndmask_b32_e64 v155, 0, 1, s[0:1]
	v_cmp_gt_u64_e64 s[0:1], s[40:41], v[148:149]
	v_readlane_b32 s13, v149, 45
	v_readlane_b32 s85, v149, 46
	v_addc_co_u32_e64 v154, s[0:1], v154, v155, s[0:1]
	v_cmp_gt_u64_e64 s[0:1], s[34:35], v[148:149]
	v_readlane_b32 s83, v149, 47
	s_nop 0
	v_cndmask_b32_e64 v155, 0, 1, s[0:1]
	v_cmp_gt_u64_e64 s[0:1], s[2:3], v[148:149]
	s_nop 1
	v_addc_co_u32_e64 v154, s[0:1], v154, v155, s[0:1]
	v_cmp_gt_u64_e64 s[0:1], s[16:17], v[148:149]
	s_nop 1
	v_cndmask_b32_e64 v155, 0, 1, s[0:1]
	v_cmp_gt_u64_e64 s[0:1], s[12:13], v[148:149]
	s_nop 1
	v_addc_co_u32_e64 v154, s[0:1], v154, v155, s[0:1]
	v_readlane_b32 s0, v254, 60
	v_readlane_b32 s1, v254, 61
	s_mov_b32 s84, s0
	s_nop 0
	s_nop 1
	s_nop 0
	v_cmp_gt_u64_e64 s[0:1], s[84:85], v[148:149]
	s_nop 1
	v_cndmask_b32_e64 v155, 0, 1, s[0:1]
	v_cmp_gt_u64_e64 s[0:1], s[82:83], v[148:149]
	s_nop 1
	v_addc_co_u32_e64 v154, s[0:1], v154, v155, s[0:1]
	s_and_b32 s1, vcc_hi, 0x10000
	s_mov_b32 s0, s25
	s_cmp_eq_u64 s[0:1], 0
	s_cbranch_scc1 .LBB0_605
.LBB0_622:
	v_readlane_b32 s77, v149, 48
	v_readlane_b32 s7, v149, 49
	v_readlane_b32 s85, v149, 50
	v_cmp_gt_u64_e64 s[0:1], s[76:77], v[148:149]
	v_readlane_b32 s81, v149, 51
	v_readlane_b32 s71, v149, 53
	v_cndmask_b32_e64 v155, 0, 1, s[0:1]
	v_cmp_gt_u64_e64 s[0:1], s[6:7], v[148:149]
	v_readlane_b32 s89, v149, 54
	v_readlane_b32 s79, v149, 55
	v_addc_co_u32_e64 v154, s[0:1], v154, v155, s[0:1]
	v_readlane_b32 s0, v255, 6
	v_readlane_b32 s1, v255, 7
	s_mov_b32 s84, s0
	s_nop 0
	s_nop 1
	s_nop 0
	v_cmp_gt_u64_e64 s[0:1], s[84:85], v[148:149]
	v_readlane_b32 s85, v149, 52
	s_nop 0
	v_cndmask_b32_e64 v155, 0, 1, s[0:1]
	v_cmp_gt_u64_e64 s[0:1], s[80:81], v[148:149]
	s_nop 1
	v_addc_co_u32_e64 v154, s[0:1], v154, v155, s[0:1]
	v_readlane_b32 s0, v255, 8
	v_readlane_b32 s1, v255, 9
	s_mov_b32 s84, s0
	s_nop 0
	s_nop 1
	s_nop 0
	v_cmp_gt_u64_e64 s[0:1], s[84:85], v[148:149]
	s_nop 1
	v_cndmask_b32_e64 v155, 0, 1, s[0:1]
	v_cmp_gt_u64_e64 s[0:1], s[70:71], v[148:149]
	s_nop 1
	v_addc_co_u32_e64 v154, s[0:1], v154, v155, s[0:1]
	v_cmp_gt_u64_e64 s[0:1], s[88:89], v[148:149]
	s_nop 1
	v_cndmask_b32_e64 v155, 0, 1, s[0:1]
	v_cmp_gt_u64_e64 s[0:1], s[78:79], v[148:149]
	s_nop 1
	v_addc_co_u32_e64 v154, s[0:1], v154, v155, s[0:1]
	s_and_b32 s1, vcc_hi, 0x1000000
	s_mov_b32 s0, s25
	s_cmp_eq_u64 s[0:1], 0
	s_cbranch_scc0 .LBB0_606
	s_branch .LBB0_607
